# P5 layer-1 tail also converts 17920 layer-1 MoE items (L1 trims 32,32,21)
# speedup vs baseline: 1.0052x; 1.0052x over previous
.LBB0_1363:
.LBB0_1365:
.LBB0_1366:
.LBB0_1368:
.LBB0_1370:
.LBB0_1372:
.LBB0_1374:
.LBB0_1378:
.LBB0_1380:
.LBB0_1381:
.LBB0_1383:
.LBB0_1385:
.LBB0_1387:
.LBB0_1388:
.LBB0_1390:
.LBB0_1392:
.LBB0_1393:
.LBB0_1394:
.LBB0_1395:
.LBB0_1397:
.LBB0_1401:
.LBB0_1403:
.LBB0_1404:
.LBB0_1406:
.LBB0_1408:
.LBB0_1410:
.LBB0_1411:
.LBB0_1414:
.LBB0_1418:
.LBB0_1420:
.LBB0_1421:
.LBB0_1423:
.LBB0_1425:
.Lmoe_site_A:
	s_nop 1
	v_writelane_b32 v255, s0, 0
	v_writelane_b32 v255, s1, 1
	v_writelane_b32 v255, s2, 2
	v_writelane_b32 v255, s3, 3
	v_writelane_b32 v255, s4, 4
	v_writelane_b32 v255, s5, 5
	v_writelane_b32 v255, s6, 6
	v_writelane_b32 v255, s7, 7
	v_writelane_b32 v255, s8, 8
	v_writelane_b32 v255, s9, 9
	v_writelane_b32 v255, s10, 10
	v_writelane_b32 v255, s11, 11
	v_writelane_b32 v255, s12, 12
	v_writelane_b32 v255, s13, 13
	v_writelane_b32 v255, s14, 14
	v_writelane_b32 v255, s15, 15
	v_writelane_b32 v255, s16, 16
	v_writelane_b32 v255, s17, 17
	v_writelane_b32 v255, s18, 18
	v_writelane_b32 v255, s19, 19
	v_writelane_b32 v255, s20, 20
	v_writelane_b32 v255, s21, 21
	v_writelane_b32 v255, s22, 22
	v_writelane_b32 v255, s23, 23
	v_writelane_b32 v255, s24, 24
	v_writelane_b32 v255, s25, 25
	v_writelane_b32 v255, s26, 26
	v_writelane_b32 v255, s27, 27
	v_writelane_b32 v255, s28, 28
	v_writelane_b32 v255, s29, 29
	v_writelane_b32 v255, s30, 30
	v_writelane_b32 v255, s31, 31
	v_writelane_b32 v255, s32, 32
	v_writelane_b32 v255, s33, 33
	v_writelane_b32 v255, s34, 34
	v_writelane_b32 v255, s35, 35
	s_movk_i32 s0, 0
	s_movk_i32 s2, 16
	s_mov_b32 s4, 0x7800
	s_mov_b32 s5, 0xd600
	s_mov_b32 s34, 0xbc00
	s_branch .Lmoe_p4
.Lmoe_site_B:
	s_nop 1
	v_writelane_b32 v255, s0, 0
	v_writelane_b32 v255, s1, 1
	v_writelane_b32 v255, s2, 2
	v_writelane_b32 v255, s3, 3
	v_writelane_b32 v255, s4, 4
	v_writelane_b32 v255, s5, 5
	v_writelane_b32 v255, s6, 6
	v_writelane_b32 v255, s7, 7
	v_writelane_b32 v255, s8, 8
	v_writelane_b32 v255, s9, 9
	v_writelane_b32 v255, s10, 10
	v_writelane_b32 v255, s11, 11
	v_writelane_b32 v255, s12, 12
	v_writelane_b32 v255, s13, 13
	v_writelane_b32 v255, s14, 14
	v_writelane_b32 v255, s15, 15
	v_writelane_b32 v255, s16, 16
	v_writelane_b32 v255, s17, 17
	v_writelane_b32 v255, s18, 18
	v_writelane_b32 v255, s19, 19
	v_writelane_b32 v255, s20, 20
	v_writelane_b32 v255, s21, 21
	v_writelane_b32 v255, s22, 22
	v_writelane_b32 v255, s23, 23
	v_writelane_b32 v255, s24, 24
	v_writelane_b32 v255, s25, 25
	v_writelane_b32 v255, s26, 26
	v_writelane_b32 v255, s27, 27
	v_writelane_b32 v255, s28, 28
	v_writelane_b32 v255, s29, 29
	v_writelane_b32 v255, s30, 30
	v_writelane_b32 v255, s31, 31
	v_writelane_b32 v255, s32, 32
	v_writelane_b32 v255, s33, 33
	v_writelane_b32 v255, s34, 34
	v_writelane_b32 v255, s35, 35
	s_movk_i32 s0, 1
	s_movk_i32 s2, 8
	s_mov_b32 s4, 0x800
	s_mov_b32 s5, 0x5e00
	s_mov_b32 s34, 0x4e00
	s_branch .Lmoe_p4

.Lmoe_site_E:
	s_nop 1
	v_writelane_b32 v255, s0, 0
	v_writelane_b32 v255, s1, 1
	v_writelane_b32 v255, s2, 2
	v_writelane_b32 v255, s3, 3
	v_writelane_b32 v255, s4, 4
	v_writelane_b32 v255, s5, 5
	v_writelane_b32 v255, s6, 6
	v_writelane_b32 v255, s7, 7
	v_writelane_b32 v255, s8, 8
	v_writelane_b32 v255, s9, 9
	v_writelane_b32 v255, s10, 10
	v_writelane_b32 v255, s11, 11
	v_writelane_b32 v255, s12, 12
	v_writelane_b32 v255, s13, 13
	v_writelane_b32 v255, s14, 14
	v_writelane_b32 v255, s15, 15
	v_writelane_b32 v255, s16, 16
	v_writelane_b32 v255, s17, 17
	v_writelane_b32 v255, s18, 18
	v_writelane_b32 v255, s19, 19
	v_writelane_b32 v255, s20, 20
	v_writelane_b32 v255, s21, 21
	v_writelane_b32 v255, s22, 22
	v_writelane_b32 v255, s23, 23
	v_writelane_b32 v255, s24, 24
	v_writelane_b32 v255, s25, 25
	v_writelane_b32 v255, s26, 26
	v_writelane_b32 v255, s27, 27
	v_writelane_b32 v255, s28, 28
	v_writelane_b32 v255, s29, 29
	v_writelane_b32 v255, s30, 30
	v_writelane_b32 v255, s31, 31
	v_writelane_b32 v255, s32, 32
	v_writelane_b32 v255, s33, 33
	v_writelane_b32 v255, s34, 34
	v_writelane_b32 v255, s35, 35
	s_movk_i32 s0, 3
	s_movk_i32 s2, 24
	s_mov_b32 s4, 0xfc00
	s_mov_b32 s5, 0x15a00
	s_mov_b32 s34, 0x14000
	s_branch .Lmoe_p4

.Lmoe_T1_l1:
	s_movk_i32 s2, 32
	s_movk_i32 s26, 1792
	s_mov_b32 s27, 0x2a00
	s_mov_b32 s28, 0x6a00
	s_mov_b32 s29, 0x1ce00
	s_mov_b32 s32, 0x21200
	s_mov_b32 s33, 0x25600
	s_mov_b32 s5, 0xaa00
	s_mov_b32 s35, 0x6400
	s_movk_i32 s34, 10
	s_branch .Lmoe_tail
.Lmoe_site_T2:
	s_nop 1
	v_writelane_b32 v255, s0, 0
	v_writelane_b32 v255, s1, 1
	v_writelane_b32 v255, s2, 2
	v_writelane_b32 v255, s3, 3
	v_writelane_b32 v255, s4, 4
	v_writelane_b32 v255, s5, 5
	v_writelane_b32 v255, s6, 6
	v_writelane_b32 v255, s7, 7
	v_writelane_b32 v255, s8, 8
	v_writelane_b32 v255, s9, 9
	v_writelane_b32 v255, s10, 10
	v_writelane_b32 v255, s11, 11
	v_writelane_b32 v255, s12, 12
	v_writelane_b32 v255, s13, 13
	v_writelane_b32 v255, s14, 14
	v_writelane_b32 v255, s15, 15
	v_writelane_b32 v255, s16, 16
	v_writelane_b32 v255, s17, 17
	v_writelane_b32 v255, s18, 18
	v_writelane_b32 v255, s19, 19
	v_writelane_b32 v255, s20, 20
	v_writelane_b32 v255, s21, 21
	v_writelane_b32 v255, s22, 22
	v_writelane_b32 v255, s23, 23
	v_writelane_b32 v255, s24, 24
	v_writelane_b32 v255, s25, 25
	v_writelane_b32 v255, s26, 26
	v_writelane_b32 v255, s27, 27
	v_writelane_b32 v255, s28, 28
	v_writelane_b32 v255, s29, 29
	v_writelane_b32 v255, s30, 30
	v_writelane_b32 v255, s31, 31
	v_writelane_b32 v255, s32, 32
	v_writelane_b32 v255, s33, 33
	v_writelane_b32 v255, s34, 34
	v_writelane_b32 v255, s35, 35
	s_movk_i32 s0, 5
	v_readlane_b32 s20, v252, 32
	s_nop 3
	s_cmp_eq_u32 s20, 0
	s_cbranch_scc1 .Lmoe_T2_l1
	s_movk_i32 s2, 128
	s_movk_i32 s26, 1024
	s_mov_b32 s27, 0x2a00
	s_mov_b32 s28, 0x6a00
	s_mov_b32 s29, 0x1ce00
	s_mov_b32 s32, 0x21200
	s_mov_b32 s33, 0x25600
	s_mov_b32 s5, 0x4000
	s_mov_b32 s35, 0x0
	s_movk_i32 s34, 16
	s_branch .Lmoe_tail

.Lmoe_T3_l1:
	s_movk_i32 s2, 64
	s_movk_i32 s26, 1536
	s_mov_b32 s27, 0x2a00
	s_mov_b32 s28, 0x6a00
	s_mov_b32 s29, 0x1ce00
	s_mov_b32 s32, 0x21200
	s_mov_b32 s33, 0x25600
	s_mov_b32 s5, 0x6400
	s_mov_b32 s35, 0x4000
	s_movk_i32 s34, 6
	s_branch .Lmoe_tail
.Lmoe_site_T0:
.Lmoe_tail:
	s_mov_b64 s[30:31], exec
	s_mov_b64 exec, -1
	v_lshrrev_b32_e32 v16, 6, v0
	v_and_b32_e32 v17, 63, v0
	v_readlane_b32 s20, v252, 32
	v_readfirstlane_b32 s1, v16
	v_readlane_b32 s6, v253, 14
	v_readlane_b32 s7, v253, 15
	s_nop 3
	s_cmp_lt_u32 s90, s2
	s_cbranch_scc1 .Lmoe_exit
	s_sub_u32 s21, s90, s2
	s_lshl_b32 s21, s21, 3
	s_add_u32 s21, s21, s1
	s_and_b32 s22, s21, 63
	s_lshr_b32 s23, s21, 6
	s_mul_i32 s23, s23, s34
	s_lshl_b32 s23, s23, 6
	s_add_u32 s4, s35, s22
	s_add_u32 s4, s4, s23
	s_lshl_b32 s23, s34, 6
	s_add_u32 s5, s4, s23
	s_movk_i32 s26, 64
	s_branch .Lmoe_common
